# nca1: dropped the nt (non-temporal) hint from the small partial-line stores (g sigmoid dwordx4, softmax dwordx3, pi dwordx4); gamma 1KB stores keep nt
# baseline (speedup 1.0000x reference)
.LBB2_26:
	s_or_b64 exec, exec, s[0:1]
	s_add_i32 s0, 0, 0x11880
	s_movk_i32 s1, 0x1600
	v_mov_b32_e32 v6, s0
	v_mad_u32_u24 v7, v26, s1, v6
	v_lshlrev_b32_e32 v8, 2, v38
	v_add_u32_e32 v9, v7, v8
	ds_write2st64_b32 v9, v22, v23 offset1:1
	ds_write2st64_b32 v9, v24, v25 offset0:2 offset1:3
	ds_write2st64_b32 v9, v18, v19 offset0:4 offset1:5
	ds_write2st64_b32 v9, v20, v21 offset0:6 offset1:7
	ds_write2st64_b32 v9, v14, v15 offset0:8 offset1:9
	ds_write2st64_b32 v9, v16, v17 offset0:10 offset1:11
	ds_write2st64_b32 v9, v10, v11 offset0:12 offset1:13
	ds_write2st64_b32 v9, v12, v13 offset0:14 offset1:15
	ds_write2st64_b32 v9, v2, v3 offset0:16 offset1:17
	ds_write2st64_b32 v9, v4, v5 offset0:18 offset1:19
	ds_write_b32 v9, v28 offset:5120
	v_xor_b32_e32 v9, 4, v26
	v_mad_u32_u24 v6, v9, s1, v6
	v_add_u32_e32 v29, v6, v8
	s_waitcnt lgkmcnt(0)
	s_barrier
	ds_read_b32 v8, v29 offset:5120
	v_lshlrev_b32_e32 v27, 2, v59
	v_add_u32_e32 v7, v7, v27
	v_add_u32_e32 v6, v6, v27
	ds_read_b32 v141, v6 offset:4224
	ds_read_b32 v140, v7 offset:4224
	ds_read2st64_b32 v[36:37], v29 offset0:18 offset1:19
	ds_read2st64_b32 v[30:31], v29 offset0:16 offset1:17
	ds_read2st64_b32 v[32:33], v29 offset1:1
	ds_read2st64_b32 v[34:35], v29 offset0:2 offset1:3
	ds_read2st64_b32 v[40:41], v29 offset0:4 offset1:5
	ds_read2st64_b32 v[42:43], v29 offset0:6 offset1:7
	ds_read2st64_b32 v[48:49], v29 offset0:8 offset1:9
	ds_read2st64_b32 v[52:53], v29 offset0:10 offset1:11
	ds_read2st64_b32 v[54:55], v29 offset0:12 offset1:13
	ds_read2st64_b32 v[62:63], v29 offset0:14 offset1:15
	s_waitcnt lgkmcnt(12)
	v_max_f32_e32 v6, v8, v8
	v_max_f32_e32 v7, v28, v28
	v_max_f32_e32 v6, v7, v6
	v_sub_f32_e32 v7, v28, v6
	v_sub_f32_e32 v6, v8, v6
	v_exp_f32_e32 v142, v7
	v_exp_f32_e32 v143, v6
	v_lshl_add_u32 v28, v39, 2, 0
	v_add_u32_e32 v51, 0x10e00, v28
	ds_read_b128 v[6:9], v51
	s_waitcnt lgkmcnt(11)
	v_pk_mul_f32 v[140:141], v[140:141], v[142:143]
	s_nop 0
	v_add_f32_e32 v144, v140, v141
	v_rcp_f32_e32 v144, v144
	s_movk_i32 s0, 0xa0
	s_nop 0
	v_mul_f32_e32 v44, v142, v144
	v_mul_f32_e32 v46, v143, v144
	s_waitcnt lgkmcnt(8)
	v_pk_mul_f32 v[32:33], v[46:47], v[32:33] op_sel_hi:[0,1]
	v_pk_fma_f32 v[22:23], v[44:45], v[22:23], v[32:33] op_sel_hi:[0,1,1]
	v_cvt_pk_f16_f32 v32, v22, v23
	s_waitcnt lgkmcnt(7)
	v_pk_mul_f32 v[22:23], v[46:47], v[34:35] op_sel_hi:[0,1]
	v_pk_fma_f32 v[22:23], v[44:45], v[24:25], v[22:23] op_sel_hi:[0,1,1]
	v_cvt_pk_f16_f32 v33, v22, v23
	s_waitcnt lgkmcnt(6)
	v_pk_mul_f32 v[22:23], v[46:47], v[40:41] op_sel_hi:[0,1]
	v_pk_fma_f32 v[18:19], v[44:45], v[18:19], v[22:23] op_sel_hi:[0,1,1]
	v_cvt_pk_f16_f32 v34, v18, v19
	s_waitcnt lgkmcnt(5)
	v_pk_mul_f32 v[18:19], v[46:47], v[42:43] op_sel_hi:[0,1]
	v_pk_fma_f32 v[18:19], v[44:45], v[20:21], v[18:19] op_sel_hi:[0,1,1]
	v_cvt_pk_f16_f32 v35, v18, v19
	s_waitcnt lgkmcnt(4)
	v_pk_mul_f32 v[18:19], v[46:47], v[48:49] op_sel_hi:[0,1]
	v_pk_fma_f32 v[14:15], v[44:45], v[14:15], v[18:19] op_sel_hi:[0,1,1]
	v_cvt_pk_f16_f32 v40, v14, v15
	s_waitcnt lgkmcnt(3)
	v_pk_mul_f32 v[14:15], v[46:47], v[52:53] op_sel_hi:[0,1]
	v_pk_fma_f32 v[14:15], v[44:45], v[16:17], v[14:15] op_sel_hi:[0,1,1]
	v_cvt_pk_f16_f32 v41, v14, v15
	s_waitcnt lgkmcnt(2)
	v_pk_mul_f32 v[14:15], v[46:47], v[54:55] op_sel_hi:[0,1]
	v_pk_fma_f32 v[10:11], v[44:45], v[10:11], v[14:15] op_sel_hi:[0,1,1]
	v_cvt_pk_f16_f32 v42, v10, v11
	s_waitcnt lgkmcnt(0)
	v_pk_mul_f32 v[10:11], v[46:47], v[62:63] op_sel_hi:[0,1]
	v_pk_fma_f32 v[10:11], v[44:45], v[12:13], v[10:11] op_sel_hi:[0,1,1]
	v_cvt_pk_f16_f32 v43, v10, v11
	v_pk_mul_f32 v[10:11], v[46:47], v[30:31] op_sel_hi:[0,1]
	v_pk_fma_f32 v[2:3], v[44:45], v[2:3], v[10:11] op_sel_hi:[0,1,1]
	v_cvt_pk_f16_f32 v24, v2, v3
	v_pk_mul_f32 v[2:3], v[46:47], v[36:37] op_sel_hi:[0,1]
	v_pk_fma_f32 v[2:3], v[44:45], v[4:5], v[2:3] op_sel_hi:[0,1,1]
	v_or_b32_e32 v30, v39, v60
	v_cvt_pk_f16_f32 v2, v2, v3
	v_cmp_lt_u32_e32 vcc, 31, v38
	v_and_or_b32 v29, v39, 4, v60
	v_mul_u32_u24_e32 v3, 0x50, v30
	v_cndmask_b32_e64 v45, v2, 0, vcc
	v_mad_u32_u24 v2, v29, s0, 0
	v_lshlrev_b32_e32 v36, 3, v59
	v_lshlrev_b32_e32 v48, 1, v3
	v_add_u32_e32 v31, 0xe100, v2
	v_and_b32_e32 v2, 24, v36
	v_add_u32_e32 v49, 0, v48
	v_add_u32_e32 v44, v49, v2
	v_add_u32_e32 v37, v31, v2
	v_add3_u32 v25, 0, v2, v48
	ds_read_b64_tr_b16 v[12:13], v44 offset:60160
	ds_read_b64_tr_b16 v[10:11], v25 offset:57600
	ds_read_b64_tr_b16 v[14:15], v25 offset:62720
	ds_read_b64_tr_b16 v[16:17], v44 offset:65280
	ds_read_b64_tr_b16 v[2:3], v37 offset:10240
	ds_read_b64_tr_b16 v[18:19], v25 offset:57664
	ds_read_b64_tr_b16 v[22:23], v37 offset:10272
	ds_read_b64_tr_b16 v[54:55], v44 offset:60192
	ds_read_b64_tr_b16 v[20:21], v44 offset:60224
	ds_read_b64_tr_b16 v[62:63], v44 offset:60288
	s_waitcnt lgkmcnt(8)
	v_mfma_f32_16x16x32_f16 v[6:9], v[10:13], v[32:35], v[6:9]
	v_mov_b32_e32 v4, 0
	v_mov_b32_e32 v5, v4
	ds_read_b64_tr_b16 v[52:53], v25 offset:57632
	ds_read_b64_tr_b16 v[10:11], v25 offset:62784
	s_waitcnt vmcnt(1)
	ds_read_b64_tr_b16 v[66:67], v44 offset:65312
	ds_read_b64_tr_b16 v[12:13], v44 offset:65344
	ds_read_b64_tr_b16 v[70:71], v44 offset:65408
	s_waitcnt lgkmcnt(11)
	v_mfma_f32_16x16x32_f16 v[6:9], v[14:17], v[40:43], v[6:9]
	v_cndmask_b32_e64 v44, v24, 0, vcc
	v_mov_b32_e32 v46, v4
	v_mov_b32_e32 v47, v4
	v_mov_b32_e32 v24, v4
	v_or_b32_e32 v36, 0x60, v36
	s_waitcnt lgkmcnt(10)
	v_mfma_f32_16x16x32_f16 v[14:17], v[2:5], v[44:47], v[6:9]
	s_nop 2
	ds_read_b128 v[6:9], v51 offset:64
	s_waitcnt vmcnt(0)
	ds_read_b128 v[72:75], v51 offset:128
	ds_read_b64_tr_b16 v[2:3], v37 offset:10304
	ds_read_b64_tr_b16 v[64:65], v25 offset:62752
	ds_read_b64_tr_b16 v[68:69], v25 offset:62848
	ds_read_b64_tr_b16 v[60:61], v25 offset:57728
	v_mov_b32_e32 v25, v4
	s_waitcnt lgkmcnt(5)
	v_mfma_f32_16x16x32_f16 v[6:9], v[52:55], v[32:35], v[6:9]
	v_add3_u32 v48, 0, v36, v48
	v_add_u32_e32 v49, v49, v36
	s_movk_i32 s0, 0xff
	s_waitcnt lgkmcnt(2)
	v_mfma_f32_16x16x32_f16 v[6:9], v[64:67], v[40:43], v[6:9]
	v_cmp_lt_u32_e64 s[0:1], s0, v0
	v_mfma_f32_16x16x32_f16 v[22:25], v[22:25], v[44:47], v[6:9]
	v_mfma_f32_16x16x32_f16 v[6:9], v[18:21], v[32:35], v[72:75]
	ds_read_b64_tr_b16 v[18:19], v48 offset:57600
	ds_read_b64_tr_b16 v[20:21], v49 offset:60160
	v_mfma_f32_16x16x32_f16 v[6:9], v[10:13], v[40:43], v[6:9]
	v_mfma_f32_16x16x32_f16 v[10:13], v[2:5], v[44:47], v[6:9]
	v_add_u32_e32 v2, v31, v36
	s_nop 5
	ds_read_b128 v[6:9], v51 offset:192
	ds_read_b64_tr_b16 v[52:53], v48 offset:62720
	ds_read_b64_tr_b16 v[2:3], v2 offset:10240
	ds_read_b128 v[64:67], v51 offset:256
	ds_read_b64_tr_b16 v[54:55], v49 offset:65280
	s_waitcnt lgkmcnt(4)
	v_mfma_f32_16x16x32_f16 v[6:9], v[18:21], v[32:35], v[6:9]
	s_waitcnt lgkmcnt(0)
	v_mfma_f32_16x16x32_f16 v[6:9], v[52:55], v[40:43], v[6:9]
	v_mfma_f32_16x16x32_f16 v[18:21], v[2:5], v[44:47], v[6:9]
	ds_read_b64_tr_b16 v[2:3], v37 offset:10368
	v_mfma_f32_16x16x32_f16 v[6:9], v[60:63], v[32:35], v[64:67]
	v_mfma_f32_16x16x32_f16 v[6:9], v[68:71], v[40:43], v[6:9]
	s_waitcnt lgkmcnt(0)
	v_mfma_f32_16x16x32_f16 v[6:9], v[2:5], v[44:47], v[6:9]
	s_and_saveexec_b64 s[6:7], s[0:1]
	s_xor_b64 s[0:1], exec, s[6:7]
	s_cbranch_execz .LBB2_38
	v_lshlrev_b32_e32 v5, 2, v1
	s_add_i32 s6, 0, 0x10f40
	v_cvt_pk_f16_f32 v0, v14, v15
	v_add_u32_e32 v14, 0x11840, v28
	v_lshl_add_u32 v5, v5, 1, s6
	v_cvt_pk_f16_f32 v3, v24, v25
	v_cvt_pk_f16_f32 v2, v22, v23
	v_cvt_pk_f16_f32 v15, v20, v21
	v_lshl_add_u32 v28, v30, 5, v5
	ds_read_b128 v[20:23], v14
	ds_read_b64_tr_b16 v[24:25], v28
	ds_read_b64_tr_b16 v[26:27], v28 offset:512
	v_lshl_add_u32 v5, v29, 5, v5
	v_cvt_pk_f16_f32 v1, v16, v17
	v_cvt_pk_f16_f32 v14, v18, v19
	ds_read_b64_tr_b16 v[16:17], v28 offset:1024
	ds_read_b64_tr_b16 v[18:19], v28 offset:1536
	v_cvt_pk_f16_f32 v28, v6, v7
	ds_read_b64_tr_b16 v[6:7], v5 offset:2048
	s_waitcnt lgkmcnt(3)
	v_mfma_f32_16x16x32_f16 v[0:3], v[24:27], v[0:3], v[20:23]
	v_cvt_pk_f16_f32 v13, v12, v13
	v_cvt_pk_f16_f32 v12, v10, v11
	v_cvt_pk_f16_f32 v5, v8, v9
	v_mov_b32_e32 v8, v4
	v_mov_b32_e32 v9, v4
	s_waitcnt lgkmcnt(1)
	v_mfma_f32_16x16x32_f16 v[10:13], v[16:19], v[12:15], v[0:3]
	s_nop 2
	v_cndmask_b32_e64 v3, v5, 0, vcc
	v_cndmask_b32_e64 v2, v28, 0, vcc
	v_mov_b32_e32 v5, v4
	s_waitcnt lgkmcnt(0)
	s_nop 0
	v_mfma_f32_16x16x32_f16 v[0:3], v[6:9], v[2:5], v[10:13]
	s_and_saveexec_b64 s[6:7], s[2:3]
	s_xor_b64 s[2:3], exec, s[6:7]
	s_cbranch_execz .LBB2_35
	v_cmp_ne_u32_e32 vcc, 3, v50
	s_and_saveexec_b64 s[6:7], vcc
	s_cbranch_execz .LBB2_34
	v_cmp_ne_u32_e32 vcc, 1, v50
	s_and_saveexec_b64 s[8:9], vcc
	s_xor_b64 s[8:9], exec, s[8:9]
	v_lshl_add_u32 v4, v56, 1, v56
	v_mov_b32_e32 v5, 0
	v_lshl_add_u64 v[4:5], v[4:5], 2, s[4:5]
	s_mov_b64 s[10:11], 0x70000
	v_lshl_add_u64 v[4:5], v[4:5], 0, s[10:11]
	s_andn2_saveexec_b64 s[8:9], s[8:9]
	v_mul_lo_u32 v4, v56, 7
	v_mov_b32_e32 v5, 0
	v_lshl_add_u64 v[4:5], v[4:5], 2, s[4:5]
	v_lshl_add_u64 v[4:5], v[4:5], 0, 16
	s_or_b64 exec, exec, s[8:9]
	v_max3_f32 v3, v0, v1, v2
	v_sub_f32_e32 v0, v0, v3
	v_sub_f32_e32 v1, v1, v3
	v_mul_f32_e32 v0, 0x3fb8aa3b, v0
	v_mul_f32_e32 v1, 0x3fb8aa3b, v1
	v_sub_f32_e32 v2, v2, v3
	v_exp_f32_e32 v0, v0
	v_exp_f32_e32 v1, v1
	v_mul_f32_e32 v2, 0x3fb8aa3b, v2
	v_exp_f32_e32 v3, v2
	v_add_f32_e32 v2, v0, v1
	v_add_f32_e32 v2, v3, v2
	v_rcp_f32_e32 v2, v2
	s_nop 0
	v_pk_mul_f32 v[0:1], v[0:1], v[2:3] op_sel_hi:[1,0]
	v_mul_f32_e32 v2, v3, v2
	global_store_dwordx3 v[4:5], v[0:2], off

.LBB2_35:
	s_andn2_saveexec_b64 s[2:3], s[2:3]
	s_cbranch_execz .LBB2_37
	s_nop 2
	v_mul_f32_e32 v0, 0xbfb8aa3b, v0
	v_mul_f32_e32 v1, 0xbfb8aa3b, v1
	v_mul_f32_e32 v2, 0xbfb8aa3b, v2
	v_mul_f32_e32 v3, 0xbfb8aa3b, v3
	v_exp_f32_e32 v0, v0
	v_exp_f32_e32 v1, v1
	v_exp_f32_e32 v2, v2
	v_exp_f32_e32 v3, v3
	v_mul_lo_u32 v4, v56, 7
	v_mov_b32_e32 v5, 0
	v_pk_add_f32 v[0:1], v[0:1], 1.0 op_sel_hi:[1,0]
	v_pk_add_f32 v[2:3], v[2:3], 1.0 op_sel_hi:[1,0]
	v_lshl_add_u64 v[4:5], v[4:5], 2, s[4:5]
	v_rcp_f32_e32 v0, v0
	v_rcp_f32_e32 v1, v1
	v_rcp_f32_e32 v2, v2
	v_rcp_f32_e32 v3, v3
	s_nop 0
	global_store_dwordx4 v[4:5], v[0:3], off

.LBB2_38:
	s_andn2_saveexec_b64 s[0:1], s[0:1]
	s_cbranch_execz .LBB2_41
	v_and_b32_e32 v0, 3, v26
	v_mul_u32_u24_e32 v0, 0x1100, v0
	s_add_i32 s0, 0, 0x1c880
	v_mul_u32_u24_e32 v1, 0x110, v59
	v_add3_u32 v0, s0, v0, v1
	v_lshl_add_u32 v1, v39, 2, v0
	ds_write_b128 v1, v[14:17]
	ds_write_b128 v1, v[22:25] offset:64
	ds_write_b128 v1, v[10:13] offset:128
	ds_write_b128 v1, v[18:21] offset:192
	v_lshlrev_b32_e32 v1, 8, v59
	s_movk_i32 s2, 0x110
	v_sub_u32_e32 v4, v0, v1
	v_lshlrev_b32_e32 v0, 2, v27
	v_mov_b32_e32 v1, 0
	v_lshl_add_u64 v[2:3], s[4:5], 0, v[0:1]
	s_mov_b64 s[0:1], 0xa0000
	v_mad_u32_u24 v18, v50, s2, v4
	v_lshl_add_u64 v[14:15], v[2:3], 0, s[0:1]
	ds_read_b128 v[2:5], v18
	v_lshl_or_b32 v0, v58, 7, v57
	v_or3_b32 v0, v0, s28, v50
	ds_read_b128 v[10:13], v18 offset:1088
	v_lshlrev_b32_e32 v0, 6, v0
	v_lshl_add_u64 v[16:17], v[0:1], 2, v[14:15]
	s_waitcnt lgkmcnt(1)
	global_store_dwordx4 v[16:17], v[2:5], off nt
	v_or_b32_e32 v16, 0x4000, v0
	v_mov_b32_e32 v17, v1
	v_or_b32_e32 v2, 0x2000, v0
	v_mov_b32_e32 v3, v1
	v_lshl_add_u64 v[2:3], v[2:3], 2, v[14:15]
	s_waitcnt lgkmcnt(0)
	global_store_dwordx4 v[2:3], v[10:13], off nt
	ds_read_b128 v[2:5], v18 offset:2176
	ds_read_b128 v[10:13], v18 offset:3264
	v_lshl_add_u64 v[16:17], v[16:17], 2, v[14:15]
	v_or_b32_e32 v0, 0x6000, v0
	v_cmp_gt_u32_e32 vcc, 32, v38
	s_waitcnt lgkmcnt(1)
	global_store_dwordx4 v[16:17], v[2:5], off nt
	s_nop 1
	v_lshl_add_u64 v[2:3], v[0:1], 2, v[14:15]
	s_waitcnt lgkmcnt(0)
	global_store_dwordx4 v[2:3], v[10:13], off nt
	s_and_saveexec_b64 s[0:1], vcc
	s_cbranch_execz .LBB2_41
	v_lshlrev_b32_e32 v0, 3, v56
	v_lshl_add_u64 v[2:3], v[0:1], 2, s[4:5]
	v_lshlrev_b32_e32 v0, 2, v39
	v_lshl_add_u64 v[0:1], v[2:3], 0, v[0:1]
	v_add_co_u32_e32 v0, vcc, 0x4a0000, v0
	s_nop 1
	v_addc_co_u32_e32 v1, vcc, 0, v1, vcc
	global_store_dwordx4 v[0:1], v[6:9], off
